# P9 carry loads: one v_mad_u32_u24 32-bit offset + SGPR bases per step instead of two quarter-rate v_mad_i64_i32 64-bit addresses (18 steps per item)
# baseline (speedup 1.0000x reference)
.LBB0_1467:
	s_ashr_i32 s46, s53, 2
	s_mul_hi_i32 s42, s46, 0x66666667
	s_lshr_b32 s43, s42, 31
	s_ashr_i32 s42, s42, 2
	s_add_i32 s44, s42, s43
	s_mul_i32 s42, s44, 10
	s_sub_i32 s42, s46, s42
	s_lshl_b32 s42, s42, 7
	v_or_b32_e32 v100, s42, v172
	s_lshl_b32 s43, s44, 1
	s_ashr_i32 s47, s44, 4
	s_and_b32 s43, s43, 30
	v_ashrrev_i32_e32 v101, 31, v100
	s_add_i32 s55, s43, 4
	s_lshl_b32 s45, s47, 5
	s_lshl_b32 s47, s47, 2
	v_lshlrev_b64 v[102:103], 2, v[100:101]
	v_mov_b32_e32 v240, v102
	s_add_i32 s54, s45, -4
	s_add_i32 s56, s47, 0x200
	v_cmp_gt_u32_e32 vcc, s55, v1
	v_mov_b32_e32 v104, 1.0
	v_mov_b32_e32 v108, 0
	v_mov_b32_e32 v109, 0
	v_mov_b32_e32 v106, 1.0
	v_mov_b32_e32 v107, 1.0
	s_and_saveexec_b64 s[48:49], vcc
	s_cbranch_execz .LBB0_1469
	v_mov_b32_e32 v102, s54
	v_mov_b32_e32 v103, s56
	v_cndmask_b32_e64 v102, v102, v103, s[0:1]
	v_add_u32_e32 v105, v102, v1
	v_mad_u32_u24 v242, v105, s3, v240
	global_load_dwordx2 v[106:107], v242, s[16:17]
	s_nop 0
	global_load_dwordx2 v[108:109], v242, s[18:19]
.LBB0_1469:
	s_or_b64 exec, exec, s[48:49]
	v_cmp_gt_u32_e32 vcc, s55, v158
	v_mov_b32_e32 v114, 0
	v_mov_b32_e32 v116, 0
	v_mov_b32_e32 v117, 0
	v_mov_b32_e32 v105, 1.0
	s_and_saveexec_b64 s[48:49], vcc
	s_cbranch_execz .LBB0_1471
	v_mov_b32_e32 v102, s54
	v_mov_b32_e32 v103, s56
	v_cndmask_b32_e64 v102, v102, v103, s[0:1]
	v_add_u32_e32 v104, v102, v158
	v_mad_u32_u24 v242, v104, s3, v240
	global_load_dwordx2 v[104:105], v242, s[16:17]
	s_nop 0
	global_load_dwordx2 v[116:117], v242, s[18:19]
.LBB0_1471:
	s_or_b64 exec, exec, s[48:49]
	v_cmp_gt_u32_e32 vcc, s55, v159
	v_mov_b32_e32 v118, 1.0
	v_mov_b32_e32 v115, 0
	v_mov_b32_e32 v120, 1.0
	v_mov_b32_e32 v121, 1.0
	s_and_saveexec_b64 s[48:49], vcc
	s_cbranch_execz .LBB0_1473
	v_mov_b32_e32 v102, s54
	v_mov_b32_e32 v103, s56
	v_cndmask_b32_e64 v102, v102, v103, s[0:1]
	v_add_u32_e32 v114, v102, v159
	v_mad_u32_u24 v242, v114, s3, v240
	global_load_dwordx2 v[120:121], v242, s[16:17]
	s_nop 0
	global_load_dwordx2 v[114:115], v242, s[18:19]
.LBB0_1473:
	s_or_b64 exec, exec, s[48:49]
	v_cmp_gt_u32_e32 vcc, s55, v160
	v_mov_b32_e32 v122, 0
	v_mov_b32_e32 v124, 0
	v_mov_b32_e32 v125, 0
	v_mov_b32_e32 v119, 1.0
	s_and_saveexec_b64 s[48:49], vcc
	s_cbranch_execz .LBB0_1475
	v_mov_b32_e32 v102, s54
	v_mov_b32_e32 v103, s56
	v_cndmask_b32_e64 v102, v102, v103, s[0:1]
	v_add_u32_e32 v118, v102, v160
	v_mad_u32_u24 v242, v118, s3, v240
	global_load_dwordx2 v[118:119], v242, s[16:17]
	s_nop 0
	global_load_dwordx2 v[124:125], v242, s[18:19]
.LBB0_1475:
	s_or_b64 exec, exec, s[48:49]
	v_cmp_gt_u32_e32 vcc, s43, v1
	v_mov_b32_e32 v126, 1.0
	v_mov_b32_e32 v123, 0
	v_mov_b32_e32 v128, 1.0
	v_mov_b32_e32 v129, 1.0
	s_and_saveexec_b64 s[48:49], vcc
	s_cbranch_execz .LBB0_1477
	v_or_b32_e32 v122, s45, v1
	v_mad_u32_u24 v242, v122, s3, v240
	global_load_dwordx2 v[128:129], v242, s[16:17]
	s_nop 0
	global_load_dwordx2 v[122:123], v242, s[18:19]
.LBB0_1477:
	s_or_b64 exec, exec, s[48:49]
	v_cmp_gt_u32_e32 vcc, s55, v162
	v_mov_b32_e32 v130, 0
	v_mov_b32_e32 v132, 0
	v_mov_b32_e32 v133, 0
	v_mov_b32_e32 v127, 1.0
	s_and_saveexec_b64 s[48:49], vcc
	s_cbranch_execz .LBB0_1479
	v_add_u32_e32 v126, s54, v162
	v_mad_u32_u24 v242, v126, s3, v240
	global_load_dwordx2 v[126:127], v242, s[16:17]
	s_nop 0
	global_load_dwordx2 v[132:133], v242, s[18:19]
.LBB0_1479:
	s_or_b64 exec, exec, s[48:49]
	v_cmp_gt_u32_e32 vcc, s55, v163
	v_mov_b32_e32 v134, 1.0
	v_mov_b32_e32 v131, 0
	v_mov_b32_e32 v136, 1.0
	v_mov_b32_e32 v137, 1.0
	s_and_saveexec_b64 s[48:49], vcc
	s_cbranch_execz .LBB0_1481
	v_add_u32_e32 v130, s54, v163
	v_mad_u32_u24 v242, v130, s3, v240
	global_load_dwordx2 v[136:137], v242, s[16:17]
	s_nop 0
	global_load_dwordx2 v[130:131], v242, s[18:19]
.LBB0_1481:
	s_or_b64 exec, exec, s[48:49]
	v_cmp_gt_u32_e32 vcc, s55, v164
	v_mov_b32_e32 v138, 0
	v_mov_b32_e32 v140, 0
	v_mov_b32_e32 v141, 0
	v_mov_b32_e32 v135, 1.0
	s_and_saveexec_b64 s[48:49], vcc
	s_cbranch_execz .LBB0_1483
	v_add_u32_e32 v134, s54, v164
	v_mad_u32_u24 v242, v134, s3, v240
	global_load_dwordx2 v[134:135], v242, s[16:17]
	s_nop 0
	global_load_dwordx2 v[140:141], v242, s[18:19]
.LBB0_1483:
	s_or_b64 exec, exec, s[48:49]
	v_cmp_gt_u32_e32 vcc, s55, v165
	v_mov_b32_e32 v102, 1.0
	v_mov_b32_e32 v139, 0
	v_mov_b32_e32 v142, 1.0
	v_mov_b32_e32 v143, 1.0
	s_and_saveexec_b64 s[48:49], vcc
	s_cbranch_execz .LBB0_1485
	v_add_u32_e32 v103, s54, v165
	v_mad_u32_u24 v242, v103, s3, v240
	global_load_dwordx2 v[142:143], v242, s[16:17]
	global_load_dwordx2 v[138:139], v242, s[18:19]
.LBB0_1485:
	s_or_b64 exec, exec, s[48:49]
	s_waitcnt vmcnt(0)
	v_pk_fma_f32 v[108:109], v[106:107], 0, v[108:109] op_sel_hi:[1,0,1]
	s_sub_i32 s54, 34, s43
	v_pk_fma_f32 v[108:109], v[108:109], v[104:105], v[116:117]
	v_pk_mul_f32 v[104:105], v[106:107], v[104:105]
	v_pk_fma_f32 v[106:107], v[108:109], v[120:121], v[114:115]
	v_pk_mul_f32 v[104:105], v[104:105], v[120:121]
	v_pk_fma_f32 v[106:107], v[106:107], v[118:119], v[124:125]
	v_pk_mul_f32 v[104:105], v[104:105], v[118:119]
	v_pk_fma_f32 v[106:107], v[106:107], v[128:129], v[122:123]
	v_pk_mul_f32 v[104:105], v[104:105], v[128:129]
	v_pk_fma_f32 v[106:107], v[106:107], v[126:127], v[132:133]
	v_pk_mul_f32 v[104:105], v[104:105], v[126:127]
	v_pk_fma_f32 v[106:107], v[106:107], v[136:137], v[130:131]
	v_pk_mul_f32 v[104:105], v[104:105], v[136:137]
	v_pk_fma_f32 v[106:107], v[106:107], v[134:135], v[140:141]
	v_pk_mul_f32 v[104:105], v[104:105], v[134:135]
	v_pk_fma_f32 v[106:107], v[106:107], v[142:143], v[138:139]
	v_pk_mul_f32 v[104:105], v[104:105], v[142:143]
	ds_bpermute_b32 v148, v73, v104
	ds_bpermute_b32 v149, v73, v105
	ds_bpermute_b32 v152, v73, v106
	ds_bpermute_b32 v153, v73, v107
	ds_bpermute_b32 v144, v166, v104
	ds_bpermute_b32 v145, v166, v105
	ds_bpermute_b32 v150, v166, v106
	ds_bpermute_b32 v151, v166, v107
	ds_bpermute_b32 v140, v167, v104
	ds_bpermute_b32 v141, v167, v105
	ds_bpermute_b32 v146, v167, v106
	ds_bpermute_b32 v147, v167, v107
	ds_bpermute_b32 v138, v168, v104
	ds_bpermute_b32 v139, v168, v105
	ds_bpermute_b32 v142, v168, v106
	ds_bpermute_b32 v143, v168, v107
	v_lshl_add_u64 v[104:105], v[100:101], 2, v[98:99]
	v_mov_b32_e32 v241, v104
	s_add_i32 s43, s45, 35
	s_add_i32 s45, s47, 0x203
	v_cmp_gt_u32_e32 vcc, s54, v1
	v_mov_b32_e32 v104, 0
	v_mov_b32_e32 v106, 0
	v_mov_b32_e32 v107, 0
	v_mov_b32_e32 v103, 1.0
	s_and_saveexec_b64 s[48:49], vcc
	s_cbranch_execz .LBB0_1487
	v_mov_b32_e32 v102, s43
	v_mov_b32_e32 v103, s45
	v_cndmask_b32_e64 v102, v102, v103, s[0:1]
	v_sub_u32_e32 v105, v102, v1
	v_mad_u32_u24 v242, v105, s3, v241
	global_load_dwordx2 v[102:103], v242, s[16:17]
	s_nop 0
	global_load_dwordx2 v[106:107], v242, s[18:19]
.LBB0_1487:
	s_or_b64 exec, exec, s[48:49]
	v_cmp_gt_u32_e32 vcc, s54, v158
	v_mov_b32_e32 v108, 1.0
	v_mov_b32_e32 v105, 0
	v_mov_b32_e32 v110, 1.0
	v_mov_b32_e32 v111, 1.0
	s_and_saveexec_b64 s[48:49], vcc
	s_cbranch_execz .LBB0_1489
	v_mov_b32_e32 v104, s43
	v_mov_b32_e32 v105, s45
	v_cndmask_b32_e64 v104, v104, v105, s[0:1]
	v_sub_u32_e32 v109, v104, v158
	v_mad_u32_u24 v242, v109, s3, v241
	global_load_dwordx2 v[110:111], v242, s[16:17]
	s_nop 0
	global_load_dwordx2 v[104:105], v242, s[18:19]
.LBB0_1489:
	s_or_b64 exec, exec, s[48:49]
	v_cmp_gt_u32_e32 vcc, s54, v159
	v_mov_b32_e32 v112, 0
	v_mov_b32_e32 v114, 0
	v_mov_b32_e32 v115, 0
	v_mov_b32_e32 v109, 1.0
	s_and_saveexec_b64 s[48:49], vcc
	s_cbranch_execz .LBB0_1491
	v_mov_b32_e32 v108, s43
	v_mov_b32_e32 v109, s45
	v_cndmask_b32_e64 v108, v108, v109, s[0:1]
	v_sub_u32_e32 v113, v108, v159
	v_mad_u32_u24 v242, v113, s3, v241
	global_load_dwordx2 v[108:109], v242, s[16:17]
	s_nop 0
	global_load_dwordx2 v[114:115], v242, s[18:19]
.LBB0_1491:
	s_or_b64 exec, exec, s[48:49]
	v_cmp_gt_u32_e32 vcc, s54, v160
	v_mov_b32_e32 v116, 1.0
	v_mov_b32_e32 v113, 0
	v_mov_b32_e32 v118, 1.0
	v_mov_b32_e32 v119, 1.0
	s_and_saveexec_b64 s[48:49], vcc
	s_cbranch_execz .LBB0_1493
	v_mov_b32_e32 v112, s43
	v_mov_b32_e32 v113, s45
	v_cndmask_b32_e64 v112, v112, v113, s[0:1]
	v_sub_u32_e32 v117, v112, v160
	v_mad_u32_u24 v242, v117, s3, v241
	global_load_dwordx2 v[118:119], v242, s[16:17]
	s_nop 0
	global_load_dwordx2 v[112:113], v242, s[18:19]
.LBB0_1493:
	s_or_b64 exec, exec, s[48:49]
	v_cmp_gt_u32_e32 vcc, s54, v161
	v_mov_b32_e32 v120, 0
	v_mov_b32_e32 v122, 0
	v_mov_b32_e32 v123, 0
	v_mov_b32_e32 v117, 1.0
	s_and_saveexec_b64 s[48:49], vcc
	s_cbranch_execz .LBB0_1495
	v_sub_u32_e32 v121, s43, v161
	v_mad_u32_u24 v242, v121, s3, v241
	global_load_dwordx2 v[116:117], v242, s[16:17]
	s_nop 0
	global_load_dwordx2 v[122:123], v242, s[18:19]
.LBB0_1495:
	s_or_b64 exec, exec, s[48:49]
	v_cmp_gt_u32_e32 vcc, s54, v162
	v_mov_b32_e32 v124, 1.0
	v_mov_b32_e32 v121, 0
	v_mov_b32_e32 v126, 1.0
	v_mov_b32_e32 v127, 1.0
	s_and_saveexec_b64 s[48:49], vcc
	s_cbranch_execz .LBB0_1497
	v_sub_u32_e32 v125, s43, v162
	v_mad_u32_u24 v242, v125, s3, v241
	global_load_dwordx2 v[126:127], v242, s[16:17]
	s_nop 0
	global_load_dwordx2 v[120:121], v242, s[18:19]
.LBB0_1497:
	s_or_b64 exec, exec, s[48:49]
	v_cmp_gt_u32_e32 vcc, s54, v163
	v_mov_b32_e32 v128, 0
	v_mov_b32_e32 v130, 0
	v_mov_b32_e32 v131, 0
	v_mov_b32_e32 v125, 1.0
	s_and_saveexec_b64 s[48:49], vcc
	s_cbranch_execz .LBB0_1499
	v_sub_u32_e32 v129, s43, v163
	v_mad_u32_u24 v242, v129, s3, v241
	global_load_dwordx2 v[124:125], v242, s[16:17]
	s_nop 0
	global_load_dwordx2 v[130:131], v242, s[18:19]
.LBB0_1499:
	s_or_b64 exec, exec, s[48:49]
	v_cmp_gt_u32_e32 vcc, s54, v164
	v_mov_b32_e32 v132, 1.0
	v_mov_b32_e32 v129, 0
	v_mov_b32_e32 v134, 1.0
	v_mov_b32_e32 v135, 1.0
	s_and_saveexec_b64 s[48:49], vcc
	s_cbranch_execz .LBB0_1501
	v_sub_u32_e32 v133, s43, v164
	v_mad_u32_u24 v242, v133, s3, v241
	global_load_dwordx2 v[134:135], v242, s[16:17]
	s_nop 0
	global_load_dwordx2 v[128:129], v242, s[18:19]
.LBB0_1501:
	s_or_b64 exec, exec, s[48:49]
	v_cmp_gt_u32_e32 vcc, s54, v165
	v_mov_b32_e32 v136, 0
	v_mov_b32_e32 v137, 0
	v_mov_b32_e32 v133, 1.0
	s_and_saveexec_b64 s[48:49], vcc
	s_cbranch_execz .LBB0_1503
	v_sub_u32_e32 v136, s43, v165
	v_mad_u32_u24 v242, v136, s3, v241
	global_load_dwordx2 v[132:133], v242, s[16:17]
	s_nop 0
	global_load_dwordx2 v[136:137], v242, s[18:19]
